# RG-LRU: scan stage rewritten as two scalar fma/mul chains with all eight LDS reads up front (drops 12 v_mov + 7 packed ops), dead copy-back v_movs removed
# baseline (speedup 1.0000x reference)
; #define LAS __attribute__((address_space(3)))
; __device__ __forceinline__ unsigned cvtpk(float lo, float hi) { const f32x2 v = {lo, hi}; return __builtin_bit_cast(unsigned, __builtin_convertvector(v, bf16x2_t)); }
; #define LRU_LOADX(t0) do { _Pragma("unroll") for (int k = 0; k < 11; ++k) { const int trow = (t0) + 8 * wave - 3 + k; xq[k] = trow >= 0 ? xrp[((ptrdiff_t)((t0) - 3 + k)) * 512] : 0u; } \
;         _Pragma("unroll") for (int i = 0; i < 8; ++i) yv[i] = ygp[((size_t)(t0) + i) * 1024]; } while (0)
; __device__ __forceinline__ void unit(LAS unsigned char* lds, const bf16* __restrict__ xr, const bf16* __restrict__ yg, const float* __restrict__ conv_w, const float* __restrict__ conv_b, const bf16* __restrict__ wga_t, const bf16* __restrict__ wgx_t, ...
;     ...
;         { f32x2 xe[11];
; #pragma unroll
;           for (int k = 0; k < 11; ++k) xe[k] = (f32x2){__uint_as_float(xq[k] << 16), __uint_as_float(xq[k] & 0xffff0000u)};
; #pragma unroll
;           for (int i = 0; i < 8; ++i) { f32x2 xc2 = (f32x2){cb0, cb1};
; #pragma unroll
;             for (int jj = 0; jj < 4; ++jj) xc2 += (f32x2){cw0[jj], cw1[jj]} * xe[i + jj];
;             *(LAS unsigned*)(lds + XA_OFF + (8 * wave + i) * XA_P + 4 * lane) = cvtpk(xc2.x, xc2.y);
;             if ((lane >> 5) == hf) *(LAS f32x2*)(XF + (8 * wave + i) * 64 + 2 * (lane & 31)) = xc2; } }
;         bf16 ycur[8];
; #pragma unroll
;         for (int i = 0; i < 8; ++i) ycur[i] = yv[i];
;         if (t0 + 64 < SEQ) LRU_LOADX(t0 + 64);
.LBB5_937:
	v_lshlrev_b32_e32 v84, 16, v137
	v_and_b32_e32 v85, 0xffff0000, v137
	v_lshlrev_b32_e32 v88, 16, v98
	v_and_b32_e32 v89, 0xffff0000, v98
	v_pk_fma_f32 v[84:85], v[112:113], v[84:85], v[114:115]
	v_lshlrev_b32_e32 v86, 16, v138
	v_and_b32_e32 v87, 0xffff0000, v138
	v_pk_fma_f32 v[84:85], v[108:109], v[88:89], v[84:85]
	v_lshlrev_b32_e32 v82, 16, v147
	v_and_b32_e32 v83, 0xffff0000, v147
	v_pk_fma_f32 v[84:85], v[110:111], v[86:87], v[84:85]
	s_nop 0
	v_pk_fma_f32 v[84:85], v[116:117], v[82:83], v[84:85]
	s_nop 0
	v_cvt_pk_bf16_f32 v90, v84, v85
	ds_write_b32 v156, v90
	s_and_saveexec_b64 s[68:69], s[6:7]
	v_add_u32_e32 v90, s80, v128
	ds_write_b64 v90, v[84:85] offset:17408
	s_or_b64 exec, exec, s[68:69]
	v_pk_fma_f32 v[88:89], v[112:113], v[88:89], v[114:115]
	v_lshlrev_b32_e32 v84, 16, v150
	v_pk_fma_f32 v[88:89], v[108:109], v[86:87], v[88:89]
	v_and_b32_e32 v85, 0xffff0000, v150
	v_pk_fma_f32 v[88:89], v[110:111], v[82:83], v[88:89]
	v_add_u32_e32 v90, s81, v126
	v_pk_fma_f32 v[88:89], v[116:117], v[84:85], v[88:89]
	s_nop 0
	v_cvt_pk_bf16_f32 v91, v88, v89
	ds_write_b32 v90, v91
	s_and_saveexec_b64 s[68:69], s[6:7]
	v_add_u32_e32 v91, s82, v128
	ds_write_b64 v91, v[88:89] offset:17408
	s_or_b64 exec, exec, s[68:69]
	v_pk_fma_f32 v[86:87], v[112:113], v[86:87], v[114:115]
	v_lshlrev_b32_e32 v88, 16, v146
	v_pk_fma_f32 v[86:87], v[108:109], v[82:83], v[86:87]
	v_and_b32_e32 v89, 0xffff0000, v146
	v_pk_fma_f32 v[86:87], v[110:111], v[84:85], v[86:87]
	s_nop 0
	v_pk_fma_f32 v[86:87], v[116:117], v[88:89], v[86:87]
	s_nop 0
	v_cvt_pk_bf16_f32 v91, v86, v87
	ds_write_b32 v90, v91 offset:272
	s_and_saveexec_b64 s[68:69], s[6:7]
	v_add_u32_e32 v91, s83, v128
	ds_write_b64 v91, v[86:87] offset:17408
	s_or_b64 exec, exec, s[68:69]
	v_pk_fma_f32 v[82:83], v[112:113], v[82:83], v[114:115]
	v_lshlrev_b32_e32 v86, 16, v151
	v_pk_fma_f32 v[82:83], v[108:109], v[84:85], v[82:83]
	v_and_b32_e32 v87, 0xffff0000, v151
	v_pk_fma_f32 v[82:83], v[110:111], v[88:89], v[82:83]
	s_nop 0
	v_pk_fma_f32 v[82:83], v[116:117], v[86:87], v[82:83]
	s_nop 0
	v_cvt_pk_bf16_f32 v91, v82, v83
	ds_write_b32 v90, v91 offset:544
	s_and_saveexec_b64 s[68:69], s[6:7]
	v_add_u32_e32 v91, s84, v128
	ds_write_b64 v91, v[82:83] offset:17408
	s_or_b64 exec, exec, s[68:69]
	v_pk_fma_f32 v[84:85], v[112:113], v[84:85], v[114:115]
	v_lshlrev_b32_e32 v82, 16, v157
	v_pk_fma_f32 v[84:85], v[108:109], v[88:89], v[84:85]
	v_and_b32_e32 v83, 0xffff0000, v157
	v_pk_fma_f32 v[84:85], v[110:111], v[86:87], v[84:85]
	s_nop 0
	v_pk_fma_f32 v[84:85], v[116:117], v[82:83], v[84:85]
	s_nop 0
	v_cvt_pk_bf16_f32 v91, v84, v85
	ds_write_b32 v90, v91 offset:816
	s_and_saveexec_b64 s[68:69], s[6:7]
	v_add_u32_e32 v91, s85, v128
	ds_write_b64 v91, v[84:85] offset:17408
	s_or_b64 exec, exec, s[68:69]
	v_pk_fma_f32 v[88:89], v[112:113], v[88:89], v[114:115]
	v_lshlrev_b32_e32 v84, 16, v158
	v_pk_fma_f32 v[88:89], v[108:109], v[86:87], v[88:89]
	v_and_b32_e32 v85, 0xffff0000, v158
	v_pk_fma_f32 v[88:89], v[110:111], v[82:83], v[88:89]
	s_nop 0
	v_pk_fma_f32 v[88:89], v[116:117], v[84:85], v[88:89]
	s_nop 0
	v_cvt_pk_bf16_f32 v91, v88, v89
	ds_write_b32 v90, v91 offset:1088
	s_and_saveexec_b64 s[68:69], s[6:7]
	v_add_u32_e32 v91, s86, v128
	ds_write_b64 v91, v[88:89] offset:17408
	s_or_b64 exec, exec, s[68:69]
	v_pk_fma_f32 v[86:87], v[112:113], v[86:87], v[114:115]
	v_lshlrev_b32_e32 v88, 16, v159
	v_pk_fma_f32 v[86:87], v[108:109], v[82:83], v[86:87]
	v_and_b32_e32 v89, 0xffff0000, v159
	v_pk_fma_f32 v[86:87], v[110:111], v[84:85], v[86:87]
	s_nop 0
	v_pk_fma_f32 v[86:87], v[116:117], v[88:89], v[86:87]
	s_nop 0
	v_cvt_pk_bf16_f32 v91, v86, v87
	ds_write_b32 v90, v91 offset:1360
	s_and_saveexec_b64 s[68:69], s[6:7]
	v_add_u32_e32 v91, s87, v128
	ds_write_b64 v91, v[86:87] offset:17408
	s_or_b64 exec, exec, s[68:69]
	v_pk_fma_f32 v[82:83], v[112:113], v[82:83], v[114:115]
	v_lshlrev_b32_e32 v86, 16, v160
	v_pk_fma_f32 v[82:83], v[108:109], v[84:85], v[82:83]
	v_and_b32_e32 v87, 0xffff0000, v160
	v_pk_fma_f32 v[82:83], v[110:111], v[88:89], v[82:83]
	s_nop 0
	v_pk_fma_f32 v[82:83], v[116:117], v[86:87], v[82:83]
	s_nop 0
	v_cvt_pk_bf16_f32 v84, v82, v83
	ds_write_b32 v90, v84 offset:1632
	s_and_saveexec_b64 s[68:69], s[6:7]
	v_add_u32_e32 v84, s88, v128
	ds_write_b64 v84, v[82:83] offset:17408
	s_or_b64 exec, exec, s[68:69]
	s_add_i32 s90, s90, 64
	s_cmpk_gt_u32 s90, 0x7bf
	s_cselect_b64 s[68:69], -1, 0
	s_and_b64 vcc, exec, s[68:69]
	s_cbranch_vccnz .LBB5_955
	v_lshl_add_u64 v[82:83], s[22:23], 0, v[118:119]
	v_add_co_u32_e32 v84, vcc, 0x4801e000, v82
	s_nop 1
	v_addc_co_u32_e32 v85, vcc, 0, v83, vcc
	global_load_dword v137, v[84:85], off offset:2048
	v_add_co_u32_e32 v84, vcc, 0x4801f000, v82
	s_nop 1
	v_addc_co_u32_e32 v85, vcc, 0, v83, vcc
	global_load_dword v98, v[84:85], off
	global_load_dword v138, v[84:85], off offset:2048
	v_add_co_u32_e32 v84, vcc, 0x48020000, v82
	s_nop 1
	v_addc_co_u32_e32 v85, vcc, 0, v83, vcc
	global_load_dword v147, v[84:85], off
	global_load_dword v150, v[84:85], off offset:2048
	v_add_co_u32_e32 v84, vcc, 0x48021000, v82
	s_nop 1
	v_addc_co_u32_e32 v85, vcc, 0, v83, vcc
	global_load_dword v146, v[84:85], off
	global_load_dword v151, v[84:85], off offset:2048
	v_add_co_u32_e32 v84, vcc, 0x48022000, v82
	s_nop 1
	v_addc_co_u32_e32 v85, vcc, 0, v83, vcc
	v_add_co_u32_e32 v82, vcc, 0x48023000, v82
	global_load_dword v157, v[84:85], off
	global_load_dword v158, v[84:85], off offset:2048
	v_addc_co_u32_e32 v83, vcc, 0, v83, vcc
	global_load_dword v159, v[82:83], off
	global_load_dword v160, v[82:83], off offset:2048
	v_lshl_add_u64 v[82:83], s[22:23], 0, v[120:121]
	v_add_co_u32_e32 v84, vcc, 0x4c020000, v82
	s_nop 1
	v_addc_co_u32_e32 v85, vcc, 0, v83, vcc
	global_load_ushort v167, v[84:85], off
	global_load_ushort v168, v[84:85], off offset:2048
	v_add_co_u32_e32 v84, vcc, 0x4c021000, v82
	s_nop 1
	v_addc_co_u32_e32 v85, vcc, 0, v83, vcc
	global_load_ushort v169, v[84:85], off
	global_load_ushort v170, v[84:85], off offset:2048
	v_add_co_u32_e32 v84, vcc, 0x4c022000, v82
	s_nop 1
	v_addc_co_u32_e32 v85, vcc, 0, v83, vcc
	v_add_co_u32_e32 v82, vcc, 0x4c023000, v82
	global_load_ushort v172, v[84:85], off
	global_load_ushort v173, v[84:85], off offset:2048
	v_addc_co_u32_e32 v83, vcc, 0, v83, vcc
	global_load_ushort v174, v[82:83], off
	global_load_ushort v175, v[82:83], off offset:2048
; #define LAS __attribute__((address_space(3)))
; #define MFMA16(a, b, c) __builtin_amdgcn_mfma_f32_16x16x32_bf16((a), (b), (c), 0, 0, 0)
; __device__ __forceinline__ float fsig(float x) { return __builtin_amdgcn_rcpf(1.0f + __builtin_amdgcn_exp2f(-LOG2E * x)); }
; __device__ __forceinline__ void unit(LAS unsigned char* lds, const bf16* __restrict__ xr, const bf16* __restrict__ yg, const float* __restrict__ conv_w, const float* __restrict__ conv_b, const bf16* __restrict__ wga_t, const bf16* __restrict__ wgx_t, ...
;     ...
;         {
;             f32x4 ar[2] = {}, ai[2] = {};
; #pragma unroll
;             for (int ks = 0; ks < 4; ++ks) { const bf16x8 xfr = *(const LAS bf16x8*)(lds + XA_OFF + (16 * tb + l15) * XA_P + 64 * ks + 16 * l4);
; #pragma unroll
;                 for (int dt = 0; dt < 2; ++dt) { ar[dt] = MFMA16(wf[0][dt][ks], xfr, ar[dt]); ai[dt] = MFMA16(wf[1][dt][ks], xfr, ai[dt]); } }
;             const int tk = 16 * tb + l15;
; #pragma unroll
;             for (int dt = 0; dt < 2; ++dt) { const int dl = dq * 32 + 16 * dt + 4 * l4; const f32x4 xo = *(const LAS f32x4*)(XF + tk * 64 + dl); f32x4 av, bv;
; #pragma unroll
;                 for (int r = 0; r < 4; ++r) { const float rg = fsig(ar[dt][r] + cba[dt][r]), ig = fsig(ai[dt][r] + cbx[dt][r]); const float la = rg * csp[dt][r];
;                     const float a_ = __builtin_amdgcn_exp2f(LOG2E * la); av[r] = a_;
;                     bv[r] = __builtin_amdgcn_sqrtf(fmaxf(1.0f - a_ * a_, 0.f)) * (ig * xo[r]); }
;                 *(LAS f32x4*)(SA + tk * 68 + dl) = av; *(LAS f32x4*)(SB + tk * 68 + dl) = bv; }
.LBB5_955:
	s_waitcnt lgkmcnt(0)
	s_barrier
	ds_read_b128 v[82:85], v161
	ds_read_b128 v[178:181], v161 offset:64
	ds_read_b128 v[214:217], v161 offset:128
	ds_read_b128 v[218:221], v161 offset:192
	s_and_b64 vcc, exec, s[4:5]
	s_waitcnt lgkmcnt(3)
	v_mfma_f32_16x16x32_bf16 v[86:89], v[2:5], v[82:85], 0
	v_mfma_f32_16x16x32_bf16 v[90:93], v[6:9], v[82:85], 0
	v_mfma_f32_16x16x32_bf16 v[94:97], v[34:37], v[82:85], 0
	v_mfma_f32_16x16x32_bf16 v[82:85], v[38:41], v[82:85], 0
	s_waitcnt lgkmcnt(2)
	v_mfma_f32_16x16x32_bf16 v[86:89], v[10:13], v[178:181], v[86:89]
	v_mfma_f32_16x16x32_bf16 v[90:93], v[14:17], v[178:181], v[90:93]
	v_mfma_f32_16x16x32_bf16 v[94:97], v[42:45], v[178:181], v[94:97]
	v_mfma_f32_16x16x32_bf16 v[82:85], v[46:49], v[178:181], v[82:85]
	s_waitcnt lgkmcnt(1)
	v_mfma_f32_16x16x32_bf16 v[86:89], v[18:21], v[214:217], v[86:89]
	v_mfma_f32_16x16x32_bf16 v[90:93], v[22:25], v[214:217], v[90:93]
	v_mfma_f32_16x16x32_bf16 v[182:185], v[50:53], v[214:217], v[94:97]
	v_mfma_f32_16x16x32_bf16 v[82:85], v[54:57], v[214:217], v[82:85]
	s_waitcnt lgkmcnt(0)
	v_mfma_f32_16x16x32_bf16 v[186:189], v[26:29], v[218:221], v[86:89]
	v_mfma_f32_16x16x32_bf16 v[94:97], v[30:33], v[218:221], v[90:93]
	s_nop 6
	v_add_f32_e32 v124, v66, v186
	v_mul_f32_e32 v124, 0xbfb8aa3b, v124
	v_exp_f32_e32 v124, v124
	v_mfma_f32_16x16x32_bf16 v[86:89], v[58:61], v[218:221], v[182:185]
	ds_read_b128 v[90:93], v152 offset:17408
	v_add_f32_e32 v94, v70, v94
	v_add_f32_e32 v96, v72, v96
	v_mfma_f32_16x16x32_bf16 v[82:85], v[62:65], v[218:221], v[82:85]
	v_add_f32_e32 v180, v68, v188
	v_mul_f32_e32 v180, 0xbfb8aa3b, v180
	v_exp_f32_e32 v180, v180
	v_mul_f32_e32 v94, 0xbfb8aa3b, v94
	v_mul_f32_e32 v96, 0xbfb8aa3b, v96
	v_add_f32_e32 v124, 1.0, v124
	v_exp_f32_e32 v94, v94
	v_add_f32_e32 v180, 1.0, v180
	v_exp_f32_e32 v96, v96
	v_rcp_f32_e32 v125, v124
	v_rcp_f32_e32 v181, v180
	v_add_f32_e32 v94, 1.0, v94
	v_add_f32_e32 v96, 1.0, v96
	v_rcp_f32_e32 v124, v94
	v_mul_f32_e32 v94, v139, v125
	v_rcp_f32_e32 v180, v96
	v_mul_f32_e32 v96, v141, v181
	v_mul_f32_e32 v94, 0x3fb8aa3b, v94
	v_mul_f32_e32 v96, 0x3fb8aa3b, v96
	v_exp_f32_e32 v94, v94
	v_exp_f32_e32 v96, v96
	v_add_f32_e32 v95, v71, v95
	v_add_f32_e32 v97, v73, v97
	v_fma_f32 v125, -v94, v94, 1.0
	v_fma_f32 v181, -v96, v96, 1.0
	v_max_f32_e32 v125, 0, v125
	v_max_f32_e32 v181, 0, v181
	v_sqrt_f32_e32 v178, v125
	v_add_f32_e32 v125, v67, v187
	v_sqrt_f32_e32 v182, v181
	v_add_f32_e32 v181, v69, v189
	v_mul_f32_e32 v125, 0xbfb8aa3b, v125
	v_mul_f32_e32 v181, 0xbfb8aa3b, v181
	v_exp_f32_e32 v125, v125
	v_exp_f32_e32 v181, v181
	v_mul_f32_e32 v95, 0xbfb8aa3b, v95
	v_mul_f32_e32 v97, 0xbfb8aa3b, v97
	v_add_f32_e32 v125, 1.0, v125
	v_exp_f32_e32 v95, v95
	v_add_f32_e32 v181, 1.0, v181
	v_exp_f32_e32 v97, v97
	v_rcp_f32_e32 v179, v125
	v_rcp_f32_e32 v183, v181
	v_add_f32_e32 v95, 1.0, v95
	v_add_f32_e32 v97, 1.0, v97
	v_rcp_f32_e32 v125, v95
	v_mul_f32_e32 v95, v140, v179
	v_rcp_f32_e32 v181, v97
	v_mul_f32_e32 v97, v142, v183
	v_mul_f32_e32 v95, 0x3fb8aa3b, v95
	v_mul_f32_e32 v97, 0x3fb8aa3b, v97
	v_exp_f32_e32 v95, v95
	v_exp_f32_e32 v97, v97
	v_add_f32_e32 v86, v74, v86
	v_add_f32_e32 v87, v75, v87
	v_add_f32_e32 v88, v76, v88
	v_add_f32_e32 v89, v77, v89
	v_fma_f32 v179, -v95, v95, 1.0
	v_fma_f32 v183, -v97, v97, 1.0
	v_mul_f32_e32 v86, 0xbfb8aa3b, v86
	v_mul_f32_e32 v87, 0xbfb8aa3b, v87
	v_mul_f32_e32 v88, 0xbfb8aa3b, v88
	v_mul_f32_e32 v89, 0xbfb8aa3b, v89
	v_max_f32_e32 v179, 0, v179
	v_max_f32_e32 v183, 0, v183
	v_exp_f32_e32 v86, v86
	v_exp_f32_e32 v87, v87
	v_exp_f32_e32 v88, v88
	v_exp_f32_e32 v89, v89
	v_sqrt_f32_e32 v179, v179
	v_sqrt_f32_e32 v183, v183
	v_add_f32_e32 v82, v78, v82
	v_add_f32_e32 v83, v79, v83
	v_add_f32_e32 v84, v80, v84
	v_add_f32_e32 v85, v81, v85
	v_mul_f32_e32 v82, 0xbfb8aa3b, v82
	v_mul_f32_e32 v83, 0xbfb8aa3b, v83
	v_mul_f32_e32 v84, 0xbfb8aa3b, v84
	v_mul_f32_e32 v85, 0xbfb8aa3b, v85
	s_waitcnt lgkmcnt(0)
	v_pk_mul_f32 v[90:91], v[90:91], v[124:125]
	v_pk_mul_f32 v[92:93], v[92:93], v[180:181]
	v_add_f32_e32 v86, 1.0, v86
	v_exp_f32_e32 v82, v82
	v_add_f32_e32 v87, 1.0, v87
	v_exp_f32_e32 v83, v83
	v_add_f32_e32 v88, 1.0, v88
	v_exp_f32_e32 v84, v84
	v_add_f32_e32 v89, 1.0, v89
	v_exp_f32_e32 v85, v85
	v_pk_mul_f32 v[92:93], v[92:93], v[182:183]
	v_pk_mul_f32 v[90:91], v[90:91], v[178:179]
	ds_write_b128 v153, v[94:97] offset:33792
	ds_write_b128 v153, v[90:93] offset:51200
	v_rcp_f32_e32 v94, v86
	v_rcp_f32_e32 v95, v87
	v_rcp_f32_e32 v96, v88
	v_rcp_f32_e32 v97, v89
	v_add_f32_e32 v82, 1.0, v82
	v_add_f32_e32 v83, 1.0, v83
	v_add_f32_e32 v84, 1.0, v84
	v_add_f32_e32 v85, 1.0, v85
	v_rcp_f32_e32 v86, v82
	v_mul_f32_e32 v82, v143, v94
	v_rcp_f32_e32 v87, v83
	v_mul_f32_e32 v83, v144, v95
	v_rcp_f32_e32 v88, v84
	v_mul_f32_e32 v84, v145, v96
	v_rcp_f32_e32 v89, v85
	v_mul_f32_e32 v85, v107, v97
	v_mul_f32_e32 v82, 0x3fb8aa3b, v82
	v_mul_f32_e32 v83, 0x3fb8aa3b, v83
	v_mul_f32_e32 v84, 0x3fb8aa3b, v84
	v_mul_f32_e32 v85, 0x3fb8aa3b, v85
	v_exp_f32_e32 v82, v82
	v_exp_f32_e32 v83, v83
	v_exp_f32_e32 v84, v84
	v_exp_f32_e32 v85, v85
	ds_read_b128 v[90:93], v152 offset:17472
	v_fma_f32 v94, -v82, v82, 1.0
	v_fma_f32 v95, -v83, v83, 1.0
	v_fma_f32 v96, -v84, v84, 1.0
	v_fma_f32 v97, -v85, v85, 1.0
	v_max_f32_e32 v94, 0, v94
	v_max_f32_e32 v95, 0, v95
	v_max_f32_e32 v96, 0, v96
	v_max_f32_e32 v97, 0, v97
	v_sqrt_f32_e32 v94, v94
	v_sqrt_f32_e32 v95, v95
	v_sqrt_f32_e32 v96, v96
	v_sqrt_f32_e32 v97, v97
	s_waitcnt lgkmcnt(0)
	v_pk_mul_f32 v[86:87], v[90:91], v[86:87]
	v_pk_mul_f32 v[88:89], v[92:93], v[88:89]
	v_pk_mul_f32 v[86:87], v[86:87], v[94:95]
	v_pk_mul_f32 v[88:89], v[88:89], v[96:97]
	ds_write_b128 v153, v[82:85] offset:33856
	ds_write_b128 v153, v[86:89] offset:51264
	s_waitcnt lgkmcnt(0)
	s_barrier
; __device__ __forceinline__ void unit(LAS unsigned char* lds, const bf16* __restrict__ xr, const bf16* __restrict__ yg, const float* __restrict__ conv_w, const float* __restrict__ conv_b, const bf16* __restrict__ wga_t, const bf16* __restrict__ wgx_t, ...
;     ...
;         { float A = 1.f, B = 0.f;
; #pragma unroll
;             for (int i = 0; i < 8; ++i) { a8[i] = SA[(8 * sg + i) * 68 + cc]; b8[i] = SB[(8 * sg + i) * 68 + cc]; B = a8[i] * B + b8[i]; A *= a8[i]; }
;             SC[sg * 64 + cc] = (f32x2){A, B}; }
;         asm volatile("s_waitcnt lgkmcnt(0)" ::: "memory"); __builtin_amdgcn_s_barrier(); asm volatile("" ::: "memory");
;         {
;             float hcur = HS[cc];
; #pragma unroll
;             for (int s2 = 0; s2 < 7; ++s2) { const f32x2 ab = SC[s2 * 64 + cc]; if (s2 < sg) hcur = ab.x * hcur + ab.y; }
	v_add_u32_e32 v214, 0x8400, v156
	v_add_u32_e32 v215, 0xc800, v156
	v_add_u32_e32 v216, 0x8800, v156
	v_add_u32_e32 v217, 0xcc00, v156
	ds_read2_b32 v[124:125], v214 offset1:68
	ds_read2_b32 v[96:97], v215 offset1:68
	ds_read2_b32 v[94:95], v214 offset0:136 offset1:204
	ds_read2_b32 v[92:93], v215 offset0:136 offset1:204
	ds_read2_b32 v[88:89], v216 offset0:16 offset1:84
	ds_read2_b32 v[86:87], v217 offset0:16 offset1:84
	ds_read2_b32 v[84:85], v216 offset0:152 offset1:220
	ds_read2_b32 v[82:83], v217 offset0:152 offset1:220
	s_waitcnt lgkmcnt(6)
	v_fma_f32 v219, 0, v124, v96
	v_mul_f32_e32 v218, v124, v125
	v_fma_f32 v219, v219, v125, v97
	s_waitcnt lgkmcnt(4)
	v_fma_f32 v219, v219, v94, v92
	v_mul_f32_e32 v218, v218, v94
	v_fma_f32 v219, v219, v95, v93
	v_mul_f32_e32 v218, v218, v95
	s_waitcnt lgkmcnt(2)
	v_fma_f32 v219, v219, v88, v86
	v_mul_f32_e32 v218, v218, v88
	v_fma_f32 v219, v219, v89, v87
	v_mul_f32_e32 v218, v218, v89
	s_waitcnt lgkmcnt(0)
	v_fma_f32 v219, v219, v84, v82
	v_mul_f32_e32 v218, v218, v84
	v_fma_f32 v219, v219, v85, v83
	v_mul_f32_e32 v218, v218, v85
	ds_write_b64 v149, v[218:219]
	s_waitcnt lgkmcnt(0)
	s_barrier
	ds_read_b32 v90, v131
	ds_read_b64 v[214:215], v129
	ds_read_b64 v[216:217], v129 offset:512
	ds_read_b64 v[218:219], v129 offset:1024
	ds_read_b64 v[220:221], v129 offset:1536
	ds_read_b64 v[222:223], v129 offset:2048
	ds_read_b64 v[224:225], v129 offset:2560
	ds_read_b64 v[226:227], v129 offset:3072
	s_waitcnt lgkmcnt(6)
	v_fmac_f32_e32 v215, v90, v214
	v_cndmask_b32_e64 v90, v215, v90, s[4:5]
	s_waitcnt lgkmcnt(5)
	v_fmac_f32_e32 v217, v90, v216
	v_cndmask_b32_e64 v90, v90, v217, s[50:51]
	s_waitcnt lgkmcnt(4)
	v_fmac_f32_e32 v219, v90, v218
	v_cndmask_b32_e64 v90, v90, v219, s[54:55]
	s_waitcnt lgkmcnt(3)
	v_fmac_f32_e32 v221, v90, v220
	v_cndmask_b32_e64 v90, v90, v221, s[60:61]
	s_waitcnt lgkmcnt(2)
	v_fmac_f32_e32 v223, v90, v222
	v_cndmask_b32_e64 v90, v90, v223, s[62:63]
	s_waitcnt lgkmcnt(1)
	v_fmac_f32_e32 v225, v90, v224
	v_cndmask_b32_e64 v90, v90, v225, s[64:65]
	s_waitcnt lgkmcnt(0)
	v_fmac_f32_e32 v227, v90, v226
	v_cndmask_b32_e64 v90, v90, v227, s[66:67]
	s_waitcnt lgkmcnt(0)
	v_fma_f32 v96, v124, v90, v96
	v_lshlrev_b32_e32 v90, 16, v177
	v_mul_f32_e32 v91, 0x3d372713, v90
	v_mul_f32_e32 v91, v91, v90
	v_fma_f32 v91, v91, v90, v90
	v_mul_f32_e32 v91, 0x3fcc422a, v91
	v_mul_f32_e32 v91, 0xbfb8aa3b, v91
	v_exp_f32_e32 v91, v91
	v_fmac_f32_e32 v97, v125, v96
	s_mov_b32 s70, 0x9c001000
	v_fma_f32 v92, v94, v97, v92
	v_add_f32_e32 v91, 1.0, v91
	v_rcp_f32_e32 v91, v91
	v_lshlrev_b32_e32 v94, 16, v171
	v_fmac_f32_e32 v93, v95, v92
	v_fma_f32 v86, v88, v93, v86
	v_mul_f32_e32 v90, v91, v90
	v_mul_f32_e32 v177, v90, v96
	v_lshl_add_u64 v[90:91], s[22:23], 0, v[122:123]
	v_add_co_u32_e32 v178, vcc, 0x9c000000, v90
	v_cvt_pk_bf16_f32 v124, v177, s0
	s_nop 0
	v_addc_co_u32_e32 v179, vcc, 0, v91, vcc
	v_lshlrev_b32_e32 v96, 16, v176
	global_store_short v[178:179], v124, off offset:2048
	v_mul_f32_e32 v124, 0x3d372713, v96
	v_mul_f32_e32 v124, v124, v96
	v_fma_f32 v124, v124, v96, v96
	v_mul_f32_e32 v124, 0x3fcc422a, v124
	v_mul_f32_e32 v124, 0xbfb8aa3b, v124
	v_exp_f32_e32 v124, v124
	v_lshlrev_b32_e32 v88, 16, v165
	v_fmac_f32_e32 v87, v89, v86
	v_fma_f32 v82, v84, v87, v82
	v_add_f32_e32 v124, 1.0, v124
	v_rcp_f32_e32 v124, v124
	v_lshlrev_b32_e32 v84, 16, v163
	v_fmac_f32_e32 v83, v85, v82
	v_mul_f32_e32 v178, v177, v177
	v_mul_f32_e32 v96, v124, v96
	v_mul_f32_e32 v176, v96, v97
	v_add_co_u32_e32 v124, vcc, s70, v90
	v_cvt_pk_bf16_f32 v96, v176, s0
	s_nop 0
	v_addc_co_u32_e32 v125, vcc, 0, v91, vcc
	global_store_short v[124:125], v96, off offset:2048
	v_mul_f32_e32 v96, 0x3d372713, v94
	v_mul_f32_e32 v96, v96, v94
	v_fma_f32 v96, v96, v94, v94
	v_mul_f32_e32 v96, 0x3fcc422a, v96
	v_mul_f32_e32 v96, 0xbfb8aa3b, v96
	v_exp_f32_e32 v96, v96
	s_mov_b32 s70, 0x9c002000
	v_mul_f32_e32 v124, v176, v176
	v_add_f32_e32 v96, 1.0, v96
	v_rcp_f32_e32 v96, v96
	s_nop 0
	v_mul_f32_e32 v94, v96, v94
	v_mul_f32_e32 v125, v94, v92
	v_add_co_u32_e32 v96, vcc, s70, v90
	v_cvt_pk_bf16_f32 v94, v125, s0
	s_nop 0
	v_addc_co_u32_e32 v97, vcc, 0, v91, vcc
	v_lshlrev_b32_e32 v92, 16, v166
	global_store_short v[96:97], v94, off offset:2048
	v_mul_f32_e32 v94, 0x3d372713, v92
	v_mul_f32_e32 v94, v94, v92
	v_fma_f32 v94, v94, v92, v92
	v_mul_f32_e32 v94, 0x3fcc422a, v94
	v_mul_f32_e32 v94, 0xbfb8aa3b, v94
	v_exp_f32_e32 v94, v94
	s_mov_b32 s70, 0x9c003000
	v_mul_f32_e32 v96, v125, v125
	v_add_f32_e32 v94, 1.0, v94
	v_rcp_f32_e32 v94, v94
	s_nop 0
	v_mul_f32_e32 v92, v94, v92
	v_mul_f32_e32 v97, v92, v93
	v_add_co_u32_e32 v94, vcc, s70, v90
	v_cvt_pk_bf16_f32 v92, v97, s0
	s_nop 0
	v_addc_co_u32_e32 v95, vcc, 0, v91, vcc
	global_store_short v[94:95], v92, off offset:2048
	v_mul_f32_e32 v92, 0x3d372713, v88
	v_mul_f32_e32 v92, v92, v88
	v_fma_f32 v92, v92, v88, v88
	v_mul_f32_e32 v92, 0x3fcc422a, v92
	v_mul_f32_e32 v92, 0xbfb8aa3b, v92
	v_exp_f32_e32 v92, v92
	s_mov_b32 s70, 0x9c004000
	v_mul_f32_e32 v94, v97, v97
	v_add_f32_e32 v92, 1.0, v92
	v_rcp_f32_e32 v92, v92
	s_nop 0
	v_mul_f32_e32 v88, v92, v88
	v_mul_f32_e32 v95, v88, v86
	v_add_co_u32_e32 v92, vcc, s70, v90
	v_cvt_pk_bf16_f32 v88, v95, s0
	s_nop 0
	v_addc_co_u32_e32 v93, vcc, 0, v91, vcc
	v_lshlrev_b32_e32 v86, 16, v164
	global_store_short v[92:93], v88, off offset:2048
	v_mul_f32_e32 v88, 0x3d372713, v86
	v_mul_f32_e32 v88, v88, v86
	v_fma_f32 v88, v88, v86, v86
	v_mul_f32_e32 v88, 0x3fcc422a, v88
	v_mul_f32_e32 v88, 0xbfb8aa3b, v88
	v_exp_f32_e32 v88, v88
	s_mov_b32 s70, 0x9c005000
	v_mul_f32_e32 v92, v95, v95
	v_add_f32_e32 v88, 1.0, v88
	v_rcp_f32_e32 v88, v88
; __device__ __forceinline__ float bf2f(bf16 b) { return __uint_as_float(((unsigned)b) << 16); }
; __device__ __forceinline__ unsigned cvtpk(float lo, float hi) { const f32x2 v = {lo, hi}; return __builtin_bit_cast(unsigned, __builtin_convertvector(v, bf16x2_t)); }
; __device__ __forceinline__ void unit(LAS unsigned char* lds, const bf16* __restrict__ xr, const bf16* __restrict__ yg, const float* __restrict__ conv_w, const float* __restrict__ conv_b, const bf16* __restrict__ wga_t, const bf16* __restrict__ wgx_t, ...
;     ...
;             for (int i = 0; i < 8; ++i) { hcur = a8[i] * hcur + b8[i]; const float x = bf2f(ycur[i]);
;                 const float u2 = 1.5957691216f * (x + 0.044715f * x * x * x);
;                 const float y = hcur * (x * __builtin_amdgcn_rcpf(1.0f + __builtin_amdgcn_exp2f(-LOG2E * u2))); outp[((size_t)t0 + i) * DM] = (bf16)(cvtpk(y, 0.f) & 0xffffu); ysq[i] = y * y; }
; #pragma unroll
;             for (int i = 0; i < 8; ++i) { float v = ysq[i];
;                 v += __builtin_bit_cast(float, __builtin_amdgcn_update_dpp(0, __builtin_bit_cast(int, v), 0xB1, 0xf, 0xf, true));
;                 v += __builtin_bit_cast(float, __builtin_amdgcn_update_dpp(0, __builtin_bit_cast(int, v), 0x4E, 0xf, 0xf, true));
;                 v += __builtin_bit_cast(float, __builtin_amdgcn_update_dpp(0, __builtin_bit_cast(int, v), 0x141, 0xf, 0xf, true));
;                 v += __builtin_bit_cast(float, __builtin_amdgcn_update_dpp(0, __builtin_bit_cast(int, v), 0x140, 0xf, 0xf, true));
;                 v += __builtin_bit_cast(float, __builtin_amdgcn_update_dpp(0, __builtin_bit_cast(int, v), 0x142, 0xa, 0xf, false));
;                 v += __builtin_bit_cast(float, __builtin_amdgcn_update_dpp(0, __builtin_bit_cast(int, v), 0x143, 0xc, 0xf, false));
;                 ysq[i] = v; }
;             if (lane == 63) {
; #pragma unroll
;                 for (int i = 0; i < 8; ++i) ssl[((size_t)b * SEQ + t0 + 8 * sg + i) * 16 + g] = ysq[i]; }
	s_nop 0
	v_mul_f32_e32 v86, v88, v86
	v_mul_f32_e32 v93, v86, v87
	v_add_co_u32_e32 v88, vcc, s70, v90
	v_cvt_pk_bf16_f32 v86, v93, s0
	s_nop 0
	v_addc_co_u32_e32 v89, vcc, 0, v91, vcc
	global_store_short v[88:89], v86, off offset:2048
	v_mul_f32_e32 v86, 0x3d372713, v84
	v_mul_f32_e32 v86, v86, v84
	v_fma_f32 v86, v86, v84, v84
	v_mul_f32_e32 v86, 0x3fcc422a, v86
	v_mul_f32_e32 v86, 0xbfb8aa3b, v86
	v_exp_f32_e32 v86, v86
	s_mov_b32 s70, 0x9c006000
	v_mul_f32_e32 v164, v93, v93
	v_mov_b32_dpp v89, v94 quad_perm:[1,0,3,2] row_mask:0xf bank_mask:0xf bound_ctrl:1
	v_add_f32_e32 v86, 1.0, v86
	v_rcp_f32_e32 v86, v86
	v_fmac_f32_e32 v89, v97, v97
	v_mov_b32_dpp v94, v164 quad_perm:[1,0,3,2] row_mask:0xf bank_mask:0xf bound_ctrl:1
	v_fmac_f32_e32 v94, v93, v93
	v_mul_f32_e32 v84, v86, v84
	v_mul_f32_e32 v163, v84, v82
	v_add_co_u32_e32 v86, vcc, s70, v90
	v_cvt_pk_bf16_f32 v84, v163, s0
	s_nop 0
	v_addc_co_u32_e32 v87, vcc, 0, v91, vcc
	v_lshlrev_b32_e32 v82, 16, v162
	global_store_short v[86:87], v84, off offset:2048
	v_mul_f32_e32 v84, 0x3d372713, v82
	v_mul_f32_e32 v84, v84, v82
	v_fma_f32 v84, v84, v82, v82
	v_mul_f32_e32 v84, 0x3fcc422a, v84
	v_mul_f32_e32 v84, 0xbfb8aa3b, v84
	v_exp_f32_e32 v84, v84
	s_mov_b32 s70, 0x9c007000
	v_mul_f32_e32 v165, v163, v163
	v_mov_b32_dpp v87, v96 quad_perm:[1,0,3,2] row_mask:0xf bank_mask:0xf bound_ctrl:1
	v_add_f32_e32 v84, 1.0, v84
	v_rcp_f32_e32 v84, v84
	v_fmac_f32_e32 v87, v125, v125
	v_add_f32_dpp v89, v89, v89 quad_perm:[2,3,0,1] row_mask:0xf bank_mask:0xf bound_ctrl:1
	v_add_f32_dpp v93, v94, v94 quad_perm:[2,3,0,1] row_mask:0xf bank_mask:0xf bound_ctrl:1
	v_mul_f32_e32 v82, v84, v82
	v_mul_f32_e32 v162, v82, v83
	v_add_co_u32_e32 v84, vcc, s70, v90
	v_cvt_pk_bf16_f32 v82, v162, s0
	s_nop 0
	v_addc_co_u32_e32 v85, vcc, 0, v91, vcc
	v_mul_f32_e32 v166, v162, v162
	v_mov_b32_dpp v91, v92 quad_perm:[1,0,3,2] row_mask:0xf bank_mask:0xf bound_ctrl:1
	global_store_short v[84:85], v82, off offset:2048
	v_mov_b32_dpp v82, v178 quad_perm:[1,0,3,2] row_mask:0xf bank_mask:0xf bound_ctrl:1
	v_mov_b32_dpp v85, v124 quad_perm:[1,0,3,2] row_mask:0xf bank_mask:0xf bound_ctrl:1
	v_fmac_f32_e32 v91, v95, v95
	v_mov_b32_dpp v95, v165 quad_perm:[1,0,3,2] row_mask:0xf bank_mask:0xf bound_ctrl:1
	v_mov_b32_dpp v97, v166 quad_perm:[1,0,3,2] row_mask:0xf bank_mask:0xf bound_ctrl:1
	v_fmac_f32_e32 v82, v177, v177
	v_fmac_f32_e32 v85, v176, v176
	v_fmac_f32_e32 v95, v163, v163
	v_fmac_f32_e32 v97, v162, v162
	v_add_f32_dpp v82, v82, v82 quad_perm:[2,3,0,1] row_mask:0xf bank_mask:0xf bound_ctrl:1
	v_add_f32_dpp v85, v85, v85 quad_perm:[2,3,0,1] row_mask:0xf bank_mask:0xf bound_ctrl:1
	v_add_f32_dpp v87, v87, v87 quad_perm:[2,3,0,1] row_mask:0xf bank_mask:0xf bound_ctrl:1
	v_add_f32_dpp v91, v91, v91 quad_perm:[2,3,0,1] row_mask:0xf bank_mask:0xf bound_ctrl:1
	v_add_f32_dpp v95, v95, v95 quad_perm:[2,3,0,1] row_mask:0xf bank_mask:0xf bound_ctrl:1
	v_add_f32_dpp v97, v97, v97 quad_perm:[2,3,0,1] row_mask:0xf bank_mask:0xf bound_ctrl:1
	v_add_f32_dpp v82, v82, v82 row_half_mirror row_mask:0xf bank_mask:0xf bound_ctrl:1
	v_add_f32_dpp v85, v85, v85 row_half_mirror row_mask:0xf bank_mask:0xf bound_ctrl:1
	v_add_f32_dpp v87, v87, v87 row_half_mirror row_mask:0xf bank_mask:0xf bound_ctrl:1
	v_add_f32_dpp v89, v89, v89 row_half_mirror row_mask:0xf bank_mask:0xf bound_ctrl:1
	v_add_f32_dpp v91, v91, v91 row_half_mirror row_mask:0xf bank_mask:0xf bound_ctrl:1
	v_add_f32_dpp v93, v93, v93 row_half_mirror row_mask:0xf bank_mask:0xf bound_ctrl:1
	v_add_f32_dpp v95, v95, v95 row_half_mirror row_mask:0xf bank_mask:0xf bound_ctrl:1
	v_add_f32_dpp v97, v97, v97 row_half_mirror row_mask:0xf bank_mask:0xf bound_ctrl:1
	v_add_f32_dpp v82, v82, v82 row_mirror row_mask:0xf bank_mask:0xf bound_ctrl:1
	v_add_f32_dpp v85, v85, v85 row_mirror row_mask:0xf bank_mask:0xf bound_ctrl:1
	v_add_f32_dpp v87, v87, v87 row_mirror row_mask:0xf bank_mask:0xf bound_ctrl:1
	v_add_f32_dpp v89, v89, v89 row_mirror row_mask:0xf bank_mask:0xf bound_ctrl:1
	v_add_f32_dpp v91, v91, v91 row_mirror row_mask:0xf bank_mask:0xf bound_ctrl:1
	v_add_f32_dpp v93, v93, v93 row_mirror row_mask:0xf bank_mask:0xf bound_ctrl:1
	v_add_f32_dpp v95, v95, v95 row_mirror row_mask:0xf bank_mask:0xf bound_ctrl:1
	v_add_f32_dpp v97, v97, v97 row_mirror row_mask:0xf bank_mask:0xf bound_ctrl:1
	v_add_f32_dpp v82, v82, v82 row_bcast:15 row_mask:0xa bank_mask:0xf
	v_add_f32_dpp v85, v85, v85 row_bcast:15 row_mask:0xa bank_mask:0xf
	v_add_f32_dpp v87, v87, v87 row_bcast:15 row_mask:0xa bank_mask:0xf
	v_add_f32_dpp v89, v89, v89 row_bcast:15 row_mask:0xa bank_mask:0xf
	v_add_f32_dpp v91, v91, v91 row_bcast:15 row_mask:0xa bank_mask:0xf
	v_add_f32_dpp v93, v93, v93 row_bcast:15 row_mask:0xa bank_mask:0xf
	v_add_f32_dpp v95, v95, v95 row_bcast:15 row_mask:0xa bank_mask:0xf
	v_add_f32_dpp v97, v97, v97 row_bcast:15 row_mask:0xa bank_mask:0xf
	v_add_f32_dpp v82, v82, v82 row_bcast:31 row_mask:0xc bank_mask:0xf
	v_add_f32_dpp v85, v85, v85 row_bcast:31 row_mask:0xc bank_mask:0xf
	v_add_f32_dpp v87, v87, v87 row_bcast:31 row_mask:0xc bank_mask:0xf
	v_add_f32_dpp v89, v89, v89 row_bcast:31 row_mask:0xc bank_mask:0xf
	v_add_f32_dpp v91, v91, v91 row_bcast:31 row_mask:0xc bank_mask:0xf
	v_add_f32_dpp v93, v93, v93 row_bcast:31 row_mask:0xc bank_mask:0xf
	v_add_f32_dpp v95, v95, v95 row_bcast:31 row_mask:0xc bank_mask:0xf
	v_add_f32_dpp v97, v97, v97 row_bcast:31 row_mask:0xc bank_mask:0xf
	s_and_saveexec_b64 s[70:71], s[8:9]
	s_cbranch_execz .LBB5_965
	s_add_u32 s92, s22, s34
	s_addc_u32 s93, s23, s89
	global_store_dword v99, v82, s[92:93] offset:-256
	global_store_dword v99, v85, s[92:93] offset:-192
	global_store_dword v99, v87, s[92:93] offset:-128
	global_store_dword v99, v89, s[92:93] offset:-64
	global_store_dword v99, v91, s[92:93]
	global_store_dword v99, v93, s[92:93] offset:64
	global_store_dword v99, v95, s[92:93] offset:128
	global_store_dword v99, v97, s[92:93] offset:192
